# fp8 conversion of w1 for layers 1-3 moved from the prologue into phase D of the previous layer (two 128k x 16n sub-tiles per unit and wave, loads in flight under the chunk-output compute stage)
# speedup vs baseline: 1.0320x; 1.0139x over previous
.LBB0_15:
	s_andn2_b64 vcc, exec, s[4:5]
	s_cbranch_vccnz .LBB0_17
	s_cmpk_lg_i32 s16, 0x800
	s_cbranch_scc1 .Lp0_w1_do
	s_cmp_gt_u32 s73, 0x61ff
	s_cbranch_scc1 .LBB0_17
.Lp0_w1_do:
	s_add_i32 s4, s73, 0xffffde00
	s_lshr_b32 s22, s4, 9
	s_lshl_b64 s[4:5], s[22:23], 23
	s_add_u32 s24, s18, s4
	s_addc_u32 s25, s19, s5
	s_lshl_b64 s[4:5], s[22:23], 21
	s_add_u32 s4, s26, s4
	s_addc_u32 s5, s27, s5
	s_and_b32 s51, s41, 0x7e0
	s_and_b32 s22, s43, 0x380
	s_lshl_b32 s51, s51, 2
	s_add_u32 s24, s24, s51
	v_or_b32_e32 v4, s22, v67
	s_addc_u32 s25, s25, 0
	v_lshl_add_u64 v[2:3], s[24:25], 0, v[70:71]
	v_lshlrev_b32_e32 v4, 13, v4
	v_mov_b32_e32 v5, v71
	v_lshl_add_u64 v[58:59], v[2:3], 0, v[4:5]
	v_add_co_u32_e32 v6, vcc, s47, v58
	v_mov_b32_e32 v75, v71
	s_nop 0
	v_addc_co_u32_e32 v7, vcc, 0, v59, vcc
	global_load_dwordx4 v[2:5], v[58:59], off nt
	s_nop 0
	global_load_dwordx4 v[6:9], v[6:7], off nt
	v_add_co_u32_e32 v10, vcc, s59, v58
	s_add_u32 s4, s4, s22
	s_nop 0
	v_addc_co_u32_e32 v11, vcc, 0, v59, vcc
	v_add_co_u32_e32 v14, vcc, s60, v58
	s_addc_u32 s5, s5, 0
	s_nop 0
	v_addc_co_u32_e32 v15, vcc, 0, v59, vcc
	global_load_dwordx4 v[10:13], v[10:11], off nt
	s_nop 0
	global_load_dwordx4 v[14:17], v[14:15], off nt
	v_add_co_u32_e32 v18, vcc, s52, v58
	s_waitcnt vmcnt(3)
	v_mul_f32_e32 v2, 0x42000000, v2
	v_addc_co_u32_e32 v19, vcc, 0, v59, vcc
	v_add_co_u32_e32 v22, vcc, s54, v58
	s_waitcnt vmcnt(2)
	v_mul_f32_e32 v6, 0x42000000, v6
	v_addc_co_u32_e32 v23, vcc, 0, v59, vcc
	global_load_dwordx4 v[18:21], v[18:19], off nt
	s_nop 0
	global_load_dwordx4 v[22:25], v[22:23], off nt
	v_add_co_u32_e32 v26, vcc, s61, v58
	v_cvt_pk_fp8_f32 v75, v2, v6
	s_nop 0
	v_addc_co_u32_e32 v27, vcc, 0, v59, vcc
	v_add_co_u32_e32 v30, vcc, s62, v58
	v_mul_f32_e32 v2, 0x42000000, v3
	s_nop 0
	v_addc_co_u32_e32 v31, vcc, 0, v59, vcc
	global_load_dwordx4 v[26:29], v[26:27], off nt
	s_nop 0
	global_load_dwordx4 v[30:33], v[30:31], off nt
	v_add_co_u32_e32 v34, vcc, s63, v58
	v_mul_f32_e32 v3, 0x42000000, v7
	s_nop 0
	v_addc_co_u32_e32 v35, vcc, 0, v59, vcc
	v_add_co_u32_e32 v38, vcc, s64, v58
	v_mov_b32_e32 v6, v71
	s_nop 0
	v_addc_co_u32_e32 v39, vcc, 0, v59, vcc
	global_load_dwordx4 v[34:37], v[34:35], off nt
	s_nop 0
	global_load_dwordx4 v[38:41], v[38:39], off nt
	v_add_co_u32_e32 v42, vcc, s65, v58
	v_cvt_pk_fp8_f32 v6, v2, v3
	s_nop 0
	v_addc_co_u32_e32 v43, vcc, 0, v59, vcc
	v_add_co_u32_e32 v46, vcc, s66, v58
	s_waitcnt vmcnt(7)
	v_mul_f32_e32 v2, 0x42000000, v11
	v_addc_co_u32_e32 v47, vcc, 0, v59, vcc
	global_load_dwordx4 v[42:45], v[42:43], off nt
	s_nop 0
	global_load_dwordx4 v[46:49], v[46:47], off nt
	v_add_co_u32_e32 v50, vcc, s67, v58
	s_waitcnt vmcnt(8)
	v_mul_f32_e32 v3, 0x42000000, v15
	v_addc_co_u32_e32 v51, vcc, 0, v59, vcc
	v_add_co_u32_e32 v54, vcc, s68, v58
	v_cvt_pk_fp8_f32 v6, v2, v3 op_sel:[0,0,1]
	s_nop 0
	v_addc_co_u32_e32 v55, vcc, 0, v59, vcc
	global_load_dwordx4 v[50:53], v[50:51], off nt
	s_nop 0
	global_load_dwordx4 v[54:57], v[54:55], off nt
	v_add_co_u32_e32 v60, vcc, s69, v58
	v_mul_f32_e32 v2, 0x42000000, v4
	s_nop 0
	v_addc_co_u32_e32 v61, vcc, 0, v59, vcc
	v_add_co_u32_e32 v62, vcc, s70, v58
	v_mul_f32_e32 v3, 0x42000000, v8
	s_nop 0
	v_addc_co_u32_e32 v63, vcc, 0, v59, vcc
	global_load_dwordx4 v[58:61], v[60:61], off nt
	s_nop 0
	global_load_dwordx4 v[62:65], v[62:63], off nt
	v_mov_b32_e32 v8, v71
	v_cvt_pk_fp8_f32 v8, v2, v3
	v_mul_f32_e32 v2, 0x42000000, v5
	v_mul_f32_e32 v3, 0x42000000, v9
	v_mov_b32_e32 v5, v71
	v_cvt_pk_fp8_f32 v5, v2, v3
	v_mul_f32_e32 v2, 0x42000000, v13
	v_mul_f32_e32 v3, 0x42000000, v17
	v_mul_f32_e32 v10, 0x42000000, v10
	v_mul_f32_e32 v14, 0x42000000, v14
	v_cvt_pk_fp8_f32 v5, v2, v3 op_sel:[0,0,1]
	v_mov_b32_e32 v9, v71
	v_cvt_pk_fp8_f32 v75, v10, v14 op_sel:[0,0,1]
	v_mov_b32_e32 v10, v71
	v_mov_b32_e32 v11, v71
	v_mul_f32_e32 v4, 0x42000000, v12
	v_mul_f32_e32 v7, 0x42000000, v16
	v_mov_b32_e32 v12, v71
	v_cvt_pk_fp8_f32 v8, v4, v7 op_sel:[0,0,1]
	v_mov_b32_e32 v13, v71
	s_waitcnt vmcnt(11)
	v_mul_f32_e32 v2, 0x42000000, v18
	s_waitcnt vmcnt(10)
	v_mul_f32_e32 v3, 0x42000000, v22
	v_cvt_pk_fp8_f32 v9, v2, v3
	v_mul_f32_e32 v2, 0x42000000, v19
	v_mul_f32_e32 v3, 0x42000000, v23
	v_cvt_pk_fp8_f32 v10, v2, v3
	s_waitcnt vmcnt(9)
	v_mul_f32_e32 v2, 0x42000000, v27
	s_waitcnt vmcnt(8)
	v_mul_f32_e32 v3, 0x42000000, v31
	v_cvt_pk_fp8_f32 v10, v2, v3 op_sel:[0,0,1]
	v_mul_f32_e32 v2, 0x42000000, v20
	v_mul_f32_e32 v3, 0x42000000, v24
	v_cvt_pk_fp8_f32 v11, v2, v3
	v_mul_f32_e32 v2, 0x42000000, v21
	v_mul_f32_e32 v3, 0x42000000, v25
	v_mul_f32_e32 v4, 0x42000000, v26
	v_mul_f32_e32 v7, 0x42000000, v30
	v_cvt_pk_fp8_f32 v12, v2, v3
	v_cvt_pk_fp8_f32 v9, v4, v7 op_sel:[0,0,1]
	v_mul_f32_e32 v4, 0x42000000, v28
	v_mul_f32_e32 v7, 0x42000000, v32
	v_cvt_pk_fp8_f32 v11, v4, v7 op_sel:[0,0,1]
	v_mul_f32_e32 v2, 0x42000000, v29
	v_mul_f32_e32 v3, 0x42000000, v33
	v_cvt_pk_fp8_f32 v12, v2, v3 op_sel:[0,0,1]
	ds_write2_b32 v83, v75, v9 offset1:8
	ds_write2_b32 v83, v6, v10 offset0:33 offset1:41
	ds_write2_b32 v83, v8, v11 offset0:66 offset1:74
	ds_write2_b32 v83, v5, v12 offset0:99 offset1:107
	s_waitcnt vmcnt(7)
	v_mul_f32_e32 v2, 0x42000000, v34
	s_waitcnt vmcnt(6)
	v_mul_f32_e32 v3, 0x42000000, v38
	v_mov_b32_e32 v6, v71
	v_cvt_pk_fp8_f32 v6, v2, v3
	v_mul_f32_e32 v2, 0x42000000, v35
	v_mul_f32_e32 v3, 0x42000000, v39
	v_mov_b32_e32 v7, v71
	v_cvt_pk_fp8_f32 v7, v2, v3
	s_waitcnt vmcnt(5)
	v_mul_f32_e32 v2, 0x42000000, v43
	s_waitcnt vmcnt(4)
	v_mul_f32_e32 v3, 0x42000000, v47
	v_mov_b32_e32 v8, v71
	v_cvt_pk_fp8_f32 v7, v2, v3 op_sel:[0,0,1]
	v_mul_f32_e32 v2, 0x42000000, v36
	v_mul_f32_e32 v3, 0x42000000, v40
	v_cvt_pk_fp8_f32 v8, v2, v3
	v_mul_f32_e32 v2, 0x42000000, v37
	v_mul_f32_e32 v3, 0x42000000, v41
	v_mov_b32_e32 v9, v71
	v_cvt_pk_fp8_f32 v9, v2, v3
	v_mul_f32_e32 v2, 0x42000000, v45
	v_mul_f32_e32 v3, 0x42000000, v49
	v_mov_b32_e32 v10, v71
	v_cvt_pk_fp8_f32 v9, v2, v3 op_sel:[0,0,1]
	s_waitcnt vmcnt(3)
	v_mul_f32_e32 v2, 0x42000000, v50
	s_waitcnt vmcnt(2)
	v_mul_f32_e32 v3, 0x42000000, v54
	v_cvt_pk_fp8_f32 v10, v2, v3
	v_mul_f32_e32 v2, 0x42000000, v51
	v_mul_f32_e32 v3, 0x42000000, v55
	v_mov_b32_e32 v11, v71
	v_cvt_pk_fp8_f32 v11, v2, v3
	s_waitcnt vmcnt(1)
	v_mul_f32_e32 v2, 0x42000000, v59
	s_waitcnt vmcnt(0)
	v_mul_f32_e32 v3, 0x42000000, v63
	v_mul_f32_e32 v4, 0x42000000, v42
	v_mul_f32_e32 v5, 0x42000000, v46
	v_cvt_pk_fp8_f32 v11, v2, v3 op_sel:[0,0,1]
	v_mul_f32_e32 v2, 0x42000000, v52
	v_mul_f32_e32 v3, 0x42000000, v56
	v_mov_b32_e32 v12, v71
	v_cvt_pk_fp8_f32 v6, v4, v5 op_sel:[0,0,1]
	v_mul_f32_e32 v4, 0x42000000, v44
	v_mul_f32_e32 v5, 0x42000000, v48
	v_cvt_pk_fp8_f32 v12, v2, v3
	v_mul_f32_e32 v2, 0x42000000, v53
	v_mul_f32_e32 v3, 0x42000000, v57
	v_cvt_pk_fp8_f32 v8, v4, v5 op_sel:[0,0,1]
	v_mul_f32_e32 v4, 0x42000000, v58
	v_mul_f32_e32 v5, 0x42000000, v62
	v_cvt_pk_fp8_f32 v13, v2, v3
	v_cvt_pk_fp8_f32 v10, v4, v5 op_sel:[0,0,1]
	v_mul_f32_e32 v4, 0x42000000, v60
	v_mul_f32_e32 v5, 0x42000000, v64
	v_cvt_pk_fp8_f32 v12, v4, v5 op_sel:[0,0,1]
	v_mul_f32_e32 v2, 0x42000000, v61
	v_mul_f32_e32 v3, 0x42000000, v65
	v_cvt_pk_fp8_f32 v13, v2, v3 op_sel:[0,0,1]
	ds_write2_b32 v83, v6, v10 offset0:16 offset1:24
	ds_write2_b32 v83, v7, v11 offset0:49 offset1:57
	ds_write2_b32 v83, v8, v12 offset0:82 offset1:90
	ds_write2_b32 v83, v9, v13 offset0:115 offset1:123
	s_waitcnt lgkmcnt(0)
	v_lshl_add_u64 v[10:11], s[4:5], 0, v[72:73]
	s_and_b32 s4, s45, 0x700
	s_and_b32 s5, s39, 0x80
	ds_read2_b32 v[2:3], v84 offset1:1
	ds_read2_b32 v[4:5], v84 offset0:2 offset1:3
	s_or_b32 s4, s4, s5
	s_and_b32 s5, s41, 0x60
	v_or_b32_e32 v6, s5, v1
	v_or_b32_e32 v6, s4, v6
	v_lshlrev_b32_e32 v6, 10, v6
	v_mov_b32_e32 v7, v71
	v_lshl_add_u64 v[12:13], v[10:11], 0, v[6:7]
	ds_read2_b32 v[6:7], v85 offset1:1
	ds_read2_b32 v[8:9], v86 offset1:1
	s_waitcnt lgkmcnt(2)
	global_store_dwordx4 v[12:13], v[2:5], off sc1 nt
	s_nop 1
	v_or_b32_e32 v2, s5, v69
	v_or_b32_e32 v2, s4, v2
	v_lshlrev_b32_e32 v2, 10, v2
	v_mov_b32_e32 v3, v71
	v_lshl_add_u64 v[2:3], v[10:11], 0, v[2:3]
	s_waitcnt lgkmcnt(0)
	global_store_dwordx4 v[2:3], v[6:9], off sc1 nt
	ds_read2_b32 v[2:3], v87 offset1:1
	ds_read2_b32 v[4:5], v88 offset1:1
	v_or_b32_e32 v6, s5, v78
	v_or_b32_e32 v6, s4, v6
	v_lshlrev_b32_e32 v6, 10, v6
	v_mov_b32_e32 v7, v71
	v_lshl_add_u64 v[12:13], v[10:11], 0, v[6:7]
	ds_read2_b32 v[6:7], v89 offset1:1
	ds_read2_b32 v[8:9], v90 offset1:1
	s_waitcnt lgkmcnt(2)
	global_store_dwordx4 v[12:13], v[2:5], off sc1 nt
	s_nop 1
	v_or_b32_e32 v2, s5, v79
	v_or_b32_e32 v2, s4, v2
	v_lshlrev_b32_e32 v2, 10, v2
	v_mov_b32_e32 v3, v71
	v_lshl_add_u64 v[2:3], v[10:11], 0, v[2:3]
	s_waitcnt lgkmcnt(0)
	global_store_dwordx4 v[2:3], v[6:9], off sc1 nt
	s_waitcnt lgkmcnt(0)

.LBB0_623:
	v_mul_lo_u32 v50, v176, s69
	v_add_u32_e32 v158, s53, v50
	v_and_b32_e32 v179, -16, v175
	v_add_u32_e32 v50, v158, v179
	v_mul_u32_u24_e32 v51, 0x48, v106
	s_waitcnt lgkmcnt(0)
	s_barrier
	s_cmpk_lg_i32 s29, 0x100
	s_cbranch_scc1 .Lcv_skip_i0
	s_cmp_gt_u32 s74, 2
	s_cbranch_scc1 .Lcv_skip_i0
	s_load_dwordx2 s[60:61], s[0:1], 0x68
	s_load_dwordx2 s[62:63], s[0:1], 0xa0
	v_readfirstlane_b32 s87, v0
	s_lshr_b32 s87, s87, 6
	s_lshl_b32 s88, s2, 3
	s_add_i32 s88, s88, s87
	s_lshr_b32 s96, s75, 8
	s_lshl_b32 s96, s96, 1
	s_lshl_b32 s96, s96, 11
	s_add_i32 s96, s96, s88
	s_lshr_b32 s51, s96, 10
	s_add_i32 s32, s74, 1
	s_lshl_b32 s32, s32, 5
	s_add_i32 s51, s51, s32
	s_bfe_u32 s32, s96, 0x30007
	s_and_b32 s33, s96, 0x7f
	s_lshl_b32 s92, s51, 23
	s_lshl_b32 s93, s32, 20
	s_add_u32 s92, s92, s93
	s_lshl_b32 s93, s33, 6
	s_add_u32 s96, s92, s93
	s_and_b32 s92, s33, 63
	s_lshr_b32 s92, s92, 3
	s_lshl_b32 s92, s92, 8
	s_lshr_b32 s93, s33, 6
	s_lshl_b32 s93, s93, 7
	s_or_b32 s92, s92, s93
	s_and_b32 s93, s33, 7
	s_lshl_b32 s93, s93, 4
	s_or_b32 s92, s92, s93
	s_lshl_b32 s92, s92, 10
	s_lshl_b32 s93, s32, 7
	s_add_u32 s92, s92, s93
	s_lshl_b32 s93, s51, 21
	s_add_u32 s92, s92, s93
	s_add_u32 s92, s92, 0x1f00000
	s_waitcnt lgkmcnt(0)
	s_add_u32 s60, s60, s96
	s_addc_u32 s61, s61, 0
	s_add_u32 s62, s62, s92
	s_addc_u32 s63, s63, 0
	v_and_b32_e32 v195, 63, v0
	v_lshrrev_b32_e32 v196, 2, v195
	v_and_b32_e32 v195, 3, v195
	v_lshlrev_b32_e32 v196, 15, v196
	v_lshl_or_b32 v195, v195, 4, v196
	global_load_dwordx4 v[202:205], v195, s[60:61] nt
	v_add_u32_e32 v196, 0x2000, v195
	global_load_dwordx4 v[206:209], v196, s[60:61] nt
	v_add_u32_e32 v196, 0x4000, v195
	global_load_dwordx4 v[210:213], v196, s[60:61] nt
	v_add_u32_e32 v196, 0x6000, v195
	global_load_dwordx4 v[216:219], v196, s[60:61] nt
	v_add_u32_e32 v196, 0x80000, v195
	global_load_dwordx4 v[220:223], v196, s[60:61] nt
	v_add_u32_e32 v196, 0x82000, v195
	global_load_dwordx4 v[224:227], v196, s[60:61] nt
	v_add_u32_e32 v196, 0x84000, v195
	global_load_dwordx4 v[228:231], v196, s[60:61] nt
	v_add_u32_e32 v196, 0x86000, v195
	global_load_dwordx4 v[246:249], v196, s[60:61] nt
.Lcv_skip_i0:
	ds_read_b128 v[134:137], v50
	ds_read_b128 v[102:105], v50 offset:64
	v_lshlrev_b32_e32 v50, 4, v177
	v_lshlrev_b32_e32 v51, 1, v51
	v_add3_u32 v107, s83, v50, v51
	v_add3_u32 v112, s84, v50, v51
	ds_read_b128 v[50:53], v107
	ds_read_b128 v[54:57], v112
	ds_read_b128 v[58:61], v107 offset:64
	ds_read_b128 v[62:65], v112 offset:64
	s_waitcnt lgkmcnt(3)
	v_mfma_f32_16x16x32_bf16 v[50:53], v[50:53], v[134:137], 0
	v_mul_u32_u24_e32 v106, 0x90, v106
	v_add3_u32 v160, s53, v179, v106
	s_mov_b64 s[6:7], -1
	s_waitcnt lgkmcnt(2)
	v_mfma_f32_16x16x32_bf16 v[54:57], v[54:57], v[134:137], 0
	s_and_b64 vcc, exec, s[78:79]
	s_waitcnt lgkmcnt(1)
	v_mfma_f32_16x16x32_bf16 v[74:77], v[58:61], v[102:105], v[50:53]
	s_waitcnt lgkmcnt(0)
	v_mfma_f32_16x16x32_bf16 v[70:73], v[62:65], v[102:105], v[54:57]
	s_nop 0
	ds_read_b128 v[50:53], v107 offset:2304
	s_nop 0
	ds_read_b128 v[54:57], v112 offset:2304
	ds_read_b128 v[58:61], v107 offset:2368
	ds_read_b128 v[62:65], v112 offset:2368
	s_waitcnt lgkmcnt(3)
	v_mfma_f32_16x16x32_bf16 v[50:53], v[50:53], v[134:137], 0
	s_waitcnt lgkmcnt(2)
	v_mfma_f32_16x16x32_bf16 v[54:57], v[54:57], v[134:137], 0
	s_waitcnt lgkmcnt(1)
	v_mfma_f32_16x16x32_bf16 v[82:85], v[58:61], v[102:105], v[50:53]
	s_waitcnt lgkmcnt(0)
	v_mfma_f32_16x16x32_bf16 v[78:81], v[62:65], v[102:105], v[54:57]
	s_nop 1
	ds_read_b128 v[50:53], v107 offset:4608
	s_nop 0
	ds_read_b128 v[54:57], v112 offset:4608
	ds_read_b128 v[58:61], v107 offset:4672
	ds_read_b128 v[62:65], v112 offset:4672
	s_waitcnt lgkmcnt(3)
	v_mfma_f32_16x16x32_bf16 v[50:53], v[50:53], v[134:137], 0
	s_waitcnt lgkmcnt(2)
	v_mfma_f32_16x16x32_bf16 v[54:57], v[54:57], v[134:137], 0
	s_waitcnt lgkmcnt(1)
	v_mfma_f32_16x16x32_bf16 v[90:93], v[58:61], v[102:105], v[50:53]
	s_waitcnt lgkmcnt(0)
	v_mfma_f32_16x16x32_bf16 v[86:89], v[62:65], v[102:105], v[54:57]
	s_nop 1
	ds_read_b128 v[50:53], v107 offset:6912
	s_nop 0
	ds_read_b128 v[54:57], v112 offset:6912
	ds_read_b128 v[58:61], v107 offset:6976
	ds_read_b128 v[62:65], v112 offset:6976
	s_waitcnt lgkmcnt(3)
	v_mfma_f32_16x16x32_bf16 v[50:53], v[50:53], v[134:137], 0
	s_waitcnt lgkmcnt(2)
	v_mfma_f32_16x16x32_bf16 v[54:57], v[54:57], v[134:137], 0
	s_waitcnt lgkmcnt(1)
	v_mfma_f32_16x16x32_bf16 v[98:101], v[58:61], v[102:105], v[50:53]
	s_waitcnt lgkmcnt(0)
	v_mfma_f32_16x16x32_bf16 v[94:97], v[62:65], v[102:105], v[54:57]
	s_nop 1
	ds_read_b128 v[50:53], v107 offset:9216
	s_nop 0
	ds_read_b128 v[54:57], v112 offset:9216
	ds_read_b128 v[58:61], v107 offset:9280
	ds_read_b128 v[62:65], v112 offset:9280
	s_waitcnt lgkmcnt(3)
	v_mfma_f32_16x16x32_bf16 v[50:53], v[50:53], v[134:137], 0
	s_waitcnt lgkmcnt(2)
	v_mfma_f32_16x16x32_bf16 v[54:57], v[54:57], v[134:137], 0
	s_waitcnt lgkmcnt(1)
	v_mfma_f32_16x16x32_bf16 v[58:61], v[58:61], v[102:105], v[50:53]
	s_waitcnt lgkmcnt(0)
	v_mfma_f32_16x16x32_bf16 v[54:57], v[62:65], v[102:105], v[54:57]
	s_nop 1
	ds_read_b128 v[50:53], v107 offset:11520
	ds_read_b128 v[62:65], v112 offset:11520
	s_waitcnt lgkmcnt(0)
	v_mfma_f32_16x16x32_bf16 v[108:111], v[62:65], v[134:137], 0
	ds_read_b128 v[62:65], v107 offset:11584
	ds_read_b128 v[112:115], v112 offset:11584
	ds_read_b128 v[138:141], v160 offset:32320
	v_mfma_f32_16x16x32_bf16 v[50:53], v[50:53], v[134:137], 0
	s_waitcnt lgkmcnt(2)
	v_mfma_f32_16x16x32_bf16 v[62:65], v[62:65], v[102:105], v[50:53]
	s_waitcnt lgkmcnt(1)
	v_mfma_f32_16x16x32_bf16 v[50:53], v[112:115], v[102:105], v[108:111]
	s_nop 2
	ds_read_b128 v[106:109], v160 offset:18432
	ds_read_b128 v[110:113], v160 offset:18496
	s_waitcnt lgkmcnt(1)
	v_mfma_f32_16x16x32_bf16 v[106:109], v[106:109], v[134:137], 0
	s_waitcnt lgkmcnt(0)
	v_mfma_f32_16x16x32_bf16 v[130:133], v[110:113], v[102:105], v[106:109]
	ds_read_b128 v[110:113], v160 offset:20800
	s_nop 4
	ds_read_b128 v[106:109], v160 offset:20736
	s_waitcnt lgkmcnt(0)
	v_mfma_f32_16x16x32_bf16 v[106:109], v[106:109], v[134:137], 0
	v_mfma_f32_16x16x32_bf16 v[126:129], v[110:113], v[102:105], v[106:109]
	ds_read_b128 v[110:113], v160 offset:23104
	s_nop 5
	ds_read_b128 v[106:109], v160 offset:23040
	s_waitcnt lgkmcnt(0)
	v_mfma_f32_16x16x32_bf16 v[106:109], v[106:109], v[134:137], 0
	v_mfma_f32_16x16x32_bf16 v[122:125], v[110:113], v[102:105], v[106:109]
	ds_read_b128 v[110:113], v160 offset:25408
	s_nop 5
	ds_read_b128 v[106:109], v160 offset:25344
	s_waitcnt lgkmcnt(0)
	v_mfma_f32_16x16x32_bf16 v[106:109], v[106:109], v[134:137], 0
	v_mfma_f32_16x16x32_bf16 v[118:121], v[110:113], v[102:105], v[106:109]
	ds_read_b128 v[110:113], v160 offset:27712
	s_nop 5
	ds_read_b128 v[106:109], v160 offset:27648
	s_waitcnt lgkmcnt(0)
	v_mfma_f32_16x16x32_bf16 v[106:109], v[106:109], v[134:137], 0
	v_mfma_f32_16x16x32_bf16 v[114:117], v[110:113], v[102:105], v[106:109]
	ds_read_b128 v[110:113], v160 offset:30016
	s_nop 5
	ds_read_b128 v[106:109], v160 offset:29952
	s_waitcnt lgkmcnt(0)
	v_mfma_f32_16x16x32_bf16 v[106:109], v[106:109], v[134:137], 0
	v_mfma_f32_16x16x32_bf16 v[110:113], v[110:113], v[102:105], v[106:109]
	s_nop 6
	ds_read_b128 v[106:109], v160 offset:32256
	s_waitcnt lgkmcnt(0)
	v_mfma_f32_16x16x32_bf16 v[106:109], v[106:109], v[134:137], 0
	v_mfma_f32_16x16x32_bf16 v[106:109], v[138:141], v[102:105], v[106:109]
	ds_read_b128 v[138:141], v160 offset:34560
	s_waitcnt lgkmcnt(0)
	v_mfma_f32_16x16x32_bf16 v[134:137], v[138:141], v[134:137], 0
	ds_read_b128 v[138:141], v160 offset:34624
	s_waitcnt lgkmcnt(0)
	v_mfma_f32_16x16x32_bf16 v[102:105], v[138:141], v[102:105], v[134:137]
	s_cbranch_vccz .LBB0_635
	s_cmp_lt_i32 s97, 1
	s_nop 2
	v_mov_b32_e32 v134, 0xbd3b9ca6
	s_cbranch_scc1 .LBB0_629
	s_cmp_eq_u32 s97, 1
	s_cbranch_scc1 .LBB0_627
	s_cmp_eq_u32 s97, 2
	v_mov_b32_e32 v134, 0xbbb906ce
	v_mov_b32_e32 v135, 0xbc3963dd
	s_cselect_b64 vcc, -1, 0
	v_cndmask_b32_e32 v134, v134, v135, vcc
	s_cbranch_execz .LBB0_628
	s_branch .LBB0_629

.LBB0_701:
	s_cmpk_lg_i32 s29, 0x100
	s_cbranch_scc1 .Lcv_skip_f0
	s_cmp_gt_u32 s74, 2
	s_cbranch_scc1 .Lcv_skip_f0
	s_waitcnt vmcnt(0)
	s_mov_b32 s32, 0x42000000
	s_mov_b32 s33, 0x42000000
	v_pk_mul_f32 v[202:203], v[202:203], s[32:33]
	v_pk_mul_f32 v[204:205], v[204:205], s[32:33]
	v_pk_mul_f32 v[206:207], v[206:207], s[32:33]
	v_pk_mul_f32 v[208:209], v[208:209], s[32:33]
	v_pk_mul_f32 v[210:211], v[210:211], s[32:33]
	v_pk_mul_f32 v[212:213], v[212:213], s[32:33]
	v_pk_mul_f32 v[216:217], v[216:217], s[32:33]
	v_pk_mul_f32 v[218:219], v[218:219], s[32:33]
	v_pk_mul_f32 v[220:221], v[220:221], s[32:33]
	v_pk_mul_f32 v[222:223], v[222:223], s[32:33]
	v_pk_mul_f32 v[224:225], v[224:225], s[32:33]
	v_pk_mul_f32 v[226:227], v[226:227], s[32:33]
	v_pk_mul_f32 v[228:229], v[228:229], s[32:33]
	v_pk_mul_f32 v[230:231], v[230:231], s[32:33]
	v_pk_mul_f32 v[246:247], v[246:247], s[32:33]
	v_pk_mul_f32 v[248:249], v[248:249], s[32:33]
	v_cvt_pk_fp8_f32 v202, v202, v206
	v_cvt_pk_fp8_f32 v202, v210, v216 op_sel:[0,0,1]
	v_cvt_pk_fp8_f32 v203, v203, v207
	v_cvt_pk_fp8_f32 v203, v211, v217 op_sel:[0,0,1]
	v_cvt_pk_fp8_f32 v204, v204, v208
	v_cvt_pk_fp8_f32 v204, v212, v218 op_sel:[0,0,1]
	v_cvt_pk_fp8_f32 v205, v205, v209
	v_cvt_pk_fp8_f32 v205, v213, v219 op_sel:[0,0,1]
	v_cvt_pk_fp8_f32 v220, v220, v224
	v_cvt_pk_fp8_f32 v220, v228, v246 op_sel:[0,0,1]
	v_cvt_pk_fp8_f32 v221, v221, v225
	v_cvt_pk_fp8_f32 v221, v229, v247 op_sel:[0,0,1]
	v_cvt_pk_fp8_f32 v222, v222, v226
	v_cvt_pk_fp8_f32 v222, v230, v248 op_sel:[0,0,1]
	v_cvt_pk_fp8_f32 v223, v223, v227
	v_cvt_pk_fp8_f32 v223, v231, v249 op_sel:[0,0,1]
	v_readfirstlane_b32 s87, v0
	s_lshr_b32 s87, s87, 6
	s_mul_i32 s87, s87, 0x840
	s_add_i32 s88, s53, 0x22000
	s_add_i32 s88, s88, s87
	v_and_b32_e32 v250, 63, v0
	v_and_b32_e32 v251, 3, v250
	v_mul_u32_u24_e32 v251, 0x84, v251
	v_lshrrev_b32_e32 v252, 2, v250
	v_add_u32_e32 v251, v251, v252
	v_lshl_add_u32 v251, v251, 2, s88
	ds_write2_b32 v251, v202, v220 offset0:0 offset1:16
	ds_write2_b32 v251, v203, v221 offset0:33 offset1:49
	ds_write2_b32 v251, v204, v222 offset0:66 offset1:82
	ds_write2_b32 v251, v205, v223 offset0:99 offset1:115
	v_lshrrev_b32_e32 v252, 3, v250
	v_mul_u32_u24_e32 v252, 33, v252
	v_and_b32_e32 v253, 7, v250
	v_lshl_add_u32 v252, v253, 2, v252
	v_lshl_add_u32 v252, v252, 2, s88
	v_add_u32_e32 v243, 0x420, v252
	v_lshrrev_b32_e32 v251, 3, v250
	v_lshlrev_b32_e32 v251, 10, v251
	v_lshl_or_b32 v251, v253, 4, v251
	v_add_u32_e32 v253, 0x2000, v251
	s_waitcnt lgkmcnt(0)
	ds_read2_b32 v[202:203], v252 offset1:1
	ds_read2_b32 v[204:205], v252 offset0:2 offset1:3
	ds_read2_b32 v[206:207], v243 offset1:1
	ds_read2_b32 v[208:209], v243 offset0:2 offset1:3
	s_waitcnt lgkmcnt(0)
	global_store_dwordx4 v251, v[202:205], s[62:63] sc1 nt
	global_store_dwordx4 v253, v[206:209], s[62:63] sc1 nt
.Lcv_skip_f0:
	s_cmpk_lg_i32 s29, 0x100
	s_cbranch_scc1 .Lcv_skip_i1
	s_cmp_gt_u32 s74, 2
	s_cbranch_scc1 .Lcv_skip_i1
	s_load_dwordx2 s[60:61], s[0:1], 0x68
	s_load_dwordx2 s[62:63], s[0:1], 0xa0
	v_readfirstlane_b32 s87, v0
	s_lshr_b32 s87, s87, 6
	s_lshl_b32 s88, s2, 3
	s_add_i32 s88, s88, s87
	s_lshr_b32 s96, s75, 8
	s_lshl_b32 s96, s96, 1
	s_add_i32 s96, s96, 1
	s_lshl_b32 s96, s96, 11
	s_add_i32 s96, s96, s88
	s_lshr_b32 s51, s96, 10
	s_add_i32 s32, s74, 1
	s_lshl_b32 s32, s32, 5
	s_add_i32 s51, s51, s32
	s_bfe_u32 s32, s96, 0x30007
	s_and_b32 s33, s96, 0x7f
	s_lshl_b32 s92, s51, 23
	s_lshl_b32 s93, s32, 20
	s_add_u32 s92, s92, s93
	s_lshl_b32 s93, s33, 6
	s_add_u32 s96, s92, s93
	s_and_b32 s92, s33, 63
	s_lshr_b32 s92, s92, 3
	s_lshl_b32 s92, s92, 8
	s_lshr_b32 s93, s33, 6
	s_lshl_b32 s93, s93, 7
	s_or_b32 s92, s92, s93
	s_and_b32 s93, s33, 7
	s_lshl_b32 s93, s93, 4
	s_or_b32 s92, s92, s93
	s_lshl_b32 s92, s92, 10
	s_lshl_b32 s93, s32, 7
	s_add_u32 s92, s92, s93
	s_lshl_b32 s93, s51, 21
	s_add_u32 s92, s92, s93
	s_add_u32 s92, s92, 0x1f00000
	s_waitcnt lgkmcnt(0)
	s_add_u32 s60, s60, s96
	s_addc_u32 s61, s61, 0
	s_add_u32 s62, s62, s92
	s_addc_u32 s63, s63, 0
	v_and_b32_e32 v195, 63, v0
	v_lshrrev_b32_e32 v196, 2, v195
	v_and_b32_e32 v195, 3, v195
	v_lshlrev_b32_e32 v196, 15, v196
	v_lshl_or_b32 v195, v195, 4, v196
	global_load_dwordx4 v[202:205], v195, s[60:61] nt
	v_add_u32_e32 v196, 0x2000, v195
	global_load_dwordx4 v[206:209], v196, s[60:61] nt
	v_add_u32_e32 v196, 0x4000, v195
	global_load_dwordx4 v[210:213], v196, s[60:61] nt
	v_add_u32_e32 v196, 0x6000, v195
	global_load_dwordx4 v[216:219], v196, s[60:61] nt
	v_add_u32_e32 v196, 0x80000, v195
	global_load_dwordx4 v[220:223], v196, s[60:61] nt
	v_add_u32_e32 v196, 0x82000, v195
	global_load_dwordx4 v[224:227], v196, s[60:61] nt
	v_add_u32_e32 v196, 0x84000, v195
	global_load_dwordx4 v[228:231], v196, s[60:61] nt
	v_add_u32_e32 v196, 0x86000, v195
	global_load_dwordx4 v[246:249], v196, s[60:61] nt
